# P11 routing scores: sub-key operand loads of K-steps 0-2 requested together, K-step 3 behind step 1, counted waits (were 48 dependent L2 round trips per item)
# speedup vs baseline: 1.0325x; 1.0126x over previous
; __device__ __forceinline__ void p11_route(Frame& F) {
;     ...
;         for (int c = 0; c < 2; ++c) {
;             f32x4 acc[8];
; #pragma unroll
;             for (int nt = 0; nt < 8; ++nt) acc[nt] = (f32x4){0.f, 0.f, 0.f, 0.f};
; #pragma unroll
;             for (int ks = 0; ks < 4; ++ks) { const gbf16x8 a = *(const gbf16x8*)(QRY + (size_t)(t0 + l15) * 2048 + h * 256 + c * 128 + 32 * ks + 8 * g);
; #pragma unroll
;                 for (int nt = 0; nt < 8; ++nt) acc[nt] = __builtin_amdgcn_mfma_f32_16x16x32_bf16(a, *(const gbf16x8*)(SK + ((size_t)(h * 2 + c) * PNK + 16 * nt + l15) * 128 + 32 * ks + 8 * g), acc[nt], 0, 0, 0); }
; #pragma unroll
;             for (int nt = 0; nt < 8; ++nt)
; #pragma unroll
;                 for (int r = 0; r < 4; ++r) sc[(c * 16 + 4 * g + r) * 129 + 16 * nt + l15] = acc[nt][r];
.LBB0_3214:
	s_lshl_b32 s4, s17, 1
	s_and_b32 s18, s4, -16
	s_waitcnt lgkmcnt(0)
	v_or_b32_e32 v126, s18, v150
	v_ashrrev_i32_e32 v127, 31, v126
	v_lshlrev_b64 v[126:127], 12, v[126:127]
	v_lshl_add_u64 v[126:127], v[2:3], 0, v[126:127]
	global_load_dwordx4 v[128:131], v[126:127], off
	global_load_dwordx4 v[132:135], v[4:5], off
	global_load_dwordx4 v[136:139], v[6:7], off
	global_load_dwordx4 v[140:143], v[8:9], off
	global_load_dwordx4 v[144:147], v[10:11], off
	global_load_dwordx4 v[160:163], v[12:13], off
	global_load_dwordx4 v[164:167], v[14:15], off
	global_load_dwordx4 v[168:171], v[16:17], off
	global_load_dwordx4 v[172:175], v[18:19], off
	global_load_dwordx4 v[176:179], v[126:127], off offset:64
	global_load_dwordx4 v[180:183], v[4:5], off offset:64
	global_load_dwordx4 v[184:187], v[20:21], off
	global_load_dwordx4 v[188:191], v[22:23], off
	global_load_dwordx4 v[192:195], v[24:25], off
	global_load_dwordx4 v[196:199], v[26:27], off
	global_load_dwordx4 v[200:203], v[28:29], off
	global_load_dwordx4 v[204:207], v[30:31], off
	global_load_dwordx4 v[208:211], v[32:33], off
	global_load_dwordx4 v[212:215], v[126:127], off offset:128
	global_load_dwordx4 v[216:219], v[4:5], off offset:128
	global_load_dwordx4 v[220:223], v[34:35], off
	global_load_dwordx4 v[224:227], v[36:37], off
	global_load_dwordx4 v[228:231], v[38:39], off
	global_load_dwordx4 v[232:235], v[40:41], off
	global_load_dwordx4 v[236:239], v[42:43], off
	global_load_dwordx4 v[240:243], v[44:45], off
	global_load_dwordx4 v[244:247], v[46:47], off
	s_mov_b32 s4, 0
	v_mov_b32_e32 v148, 0xff800000
	v_mov_b32_e32 v149, 0xff800000
	v_mov_b32_e32 v159, 0xff800000
	s_waitcnt vmcnt(25)
	v_mfma_f32_16x16x32_bf16 v[132:135], v[128:131], v[132:135], 0
	s_waitcnt vmcnt(24)
	v_mfma_f32_16x16x32_bf16 v[136:139], v[128:131], v[136:139], 0
	s_waitcnt vmcnt(23)
	v_mfma_f32_16x16x32_bf16 v[140:143], v[128:131], v[140:143], 0
	s_waitcnt vmcnt(22)
	v_mfma_f32_16x16x32_bf16 v[144:147], v[128:131], v[144:147], 0
	s_waitcnt vmcnt(21)
	v_mfma_f32_16x16x32_bf16 v[160:163], v[128:131], v[160:163], 0
	s_waitcnt vmcnt(20)
	v_mfma_f32_16x16x32_bf16 v[164:167], v[128:131], v[164:167], 0
	s_waitcnt vmcnt(19)
	v_mfma_f32_16x16x32_bf16 v[168:171], v[128:131], v[168:171], 0
	s_waitcnt vmcnt(18)
	v_mfma_f32_16x16x32_bf16 v[128:131], v[128:131], v[172:175], 0
	s_waitcnt vmcnt(16)
	v_mfma_f32_16x16x32_bf16 v[132:135], v[176:179], v[180:183], v[132:135]
	s_waitcnt vmcnt(15)
	v_mfma_f32_16x16x32_bf16 v[136:139], v[176:179], v[184:187], v[136:139]
	s_waitcnt vmcnt(14)
	v_mfma_f32_16x16x32_bf16 v[140:143], v[176:179], v[188:191], v[140:143]
	s_waitcnt vmcnt(13)
	v_mfma_f32_16x16x32_bf16 v[144:147], v[176:179], v[192:195], v[144:147]
	s_waitcnt vmcnt(12)
	v_mfma_f32_16x16x32_bf16 v[160:163], v[176:179], v[196:199], v[160:163]
	s_waitcnt vmcnt(11)
	v_mfma_f32_16x16x32_bf16 v[164:167], v[176:179], v[200:203], v[164:167]
	s_waitcnt vmcnt(10)
	v_mfma_f32_16x16x32_bf16 v[168:171], v[176:179], v[204:207], v[168:171]
	s_waitcnt vmcnt(9)
	v_mfma_f32_16x16x32_bf16 v[128:131], v[176:179], v[208:211], v[128:131]
	global_load_dwordx4 v[176:179], v[126:127], off offset:192
	global_load_dwordx4 v[180:183], v[4:5], off offset:192
	global_load_dwordx4 v[184:187], v[48:49], off
	global_load_dwordx4 v[188:191], v[50:51], off
	global_load_dwordx4 v[192:195], v[52:53], off
	global_load_dwordx4 v[196:199], v[54:55], off
	global_load_dwordx4 v[200:203], v[56:57], off
	global_load_dwordx4 v[204:207], v[58:59], off
	global_load_dwordx4 v[208:211], v[60:61], off
	s_waitcnt vmcnt(16)
	v_mfma_f32_16x16x32_bf16 v[132:135], v[212:215], v[216:219], v[132:135]
	s_waitcnt vmcnt(15)
	v_mfma_f32_16x16x32_bf16 v[136:139], v[212:215], v[220:223], v[136:139]
	s_waitcnt vmcnt(14)
	v_mfma_f32_16x16x32_bf16 v[140:143], v[212:215], v[224:227], v[140:143]
	s_waitcnt vmcnt(13)
	v_mfma_f32_16x16x32_bf16 v[144:147], v[212:215], v[228:231], v[144:147]
	s_waitcnt vmcnt(12)
	v_mfma_f32_16x16x32_bf16 v[160:163], v[212:215], v[232:235], v[160:163]
	s_waitcnt vmcnt(11)
	v_mfma_f32_16x16x32_bf16 v[164:167], v[212:215], v[236:239], v[164:167]
	s_waitcnt vmcnt(10)
	v_mfma_f32_16x16x32_bf16 v[168:171], v[212:215], v[240:243], v[168:171]
	s_waitcnt vmcnt(9)
	v_mfma_f32_16x16x32_bf16 v[128:131], v[212:215], v[244:247], v[128:131]
	s_waitcnt vmcnt(7)
	v_mfma_f32_16x16x32_bf16 v[132:135], v[176:179], v[180:183], v[132:135]
	s_waitcnt vmcnt(6)
	v_mfma_f32_16x16x32_bf16 v[136:139], v[176:179], v[184:187], v[136:139]
	s_waitcnt vmcnt(5)
	v_mfma_f32_16x16x32_bf16 v[140:143], v[176:179], v[188:191], v[140:143]
	s_waitcnt vmcnt(4)
	v_mfma_f32_16x16x32_bf16 v[144:147], v[176:179], v[192:195], v[144:147]
	s_waitcnt vmcnt(3)
	v_mfma_f32_16x16x32_bf16 v[160:163], v[176:179], v[196:199], v[160:163]
	s_waitcnt vmcnt(2)
	v_mfma_f32_16x16x32_bf16 v[164:167], v[176:179], v[200:203], v[164:167]
	s_waitcnt vmcnt(1)
	v_mfma_f32_16x16x32_bf16 v[168:171], v[176:179], v[204:207], v[168:171]
	s_waitcnt vmcnt(0)
; __device__ __forceinline__ void p11_route(Frame& F) {
;     ...
;             for (int ks = 0; ks < 4; ++ks) { const gbf16x8 a = *(const gbf16x8*)(QRY + (size_t)(t0 + l15) * 2048 + h * 256 + c * 128 + 32 * ks + 8 * g);
; #pragma unroll
;                 for (int nt = 0; nt < 8; ++nt) acc[nt] = __builtin_amdgcn_mfma_f32_16x16x32_bf16(a, *(const gbf16x8*)(SK + ((size_t)(h * 2 + c) * PNK + 16 * nt + l15) * 128 + 32 * ks + 8 * g), acc[nt], 0, 0, 0); }
; #pragma unroll
;             for (int nt = 0; nt < 8; ++nt)
; #pragma unroll
;                 for (int r = 0; r < 4; ++r) sc[(c * 16 + 4 * g + r) * 129 + 16 * nt + l15] = acc[nt][r];
	v_mfma_f32_16x16x32_bf16 v[128:131], v[176:179], v[208:211], v[128:131]
	s_nop 3
	ds_write2_b32 v151, v132, v136 offset1:16
	ds_write2_b32 v151, v133, v137 offset0:129 offset1:145
	v_add_u32_e32 v132, 0x400, v151
	ds_write2_b32 v132, v134, v138 offset0:2 offset1:18
	ds_write2_b32 v132, v135, v139 offset0:131 offset1:147
	ds_write2_b32 v151, v140, v144 offset0:32 offset1:48
	ds_write2_b32 v151, v141, v145 offset0:161 offset1:177
	ds_write2_b32 v132, v142, v146 offset0:34 offset1:50
	ds_write2_b32 v132, v143, v147 offset0:163 offset1:179
	ds_write2_b32 v151, v160, v164 offset0:64 offset1:80
	ds_write2_b32 v151, v161, v165 offset0:193 offset1:209
	ds_write2_b32 v132, v162, v166 offset0:66 offset1:82
	ds_write2_b32 v132, v163, v167 offset0:195 offset1:211
	ds_write2_b32 v151, v168, v128 offset0:96 offset1:112
	ds_write2_b32 v151, v169, v129 offset0:225 offset1:241
	ds_write2_b32 v132, v170, v130 offset0:98 offset1:114
	ds_write2_b32 v132, v171, v131 offset0:227 offset1:243
	global_load_dwordx4 v[128:131], v[126:127], off offset:256
	global_load_dwordx4 v[132:135], v[62:63], off
	global_load_dwordx4 v[136:139], v[64:65], off
	global_load_dwordx4 v[140:143], v[66:67], off
	global_load_dwordx4 v[144:147], v[68:69], off
	global_load_dwordx4 v[160:163], v[70:71], off
	global_load_dwordx4 v[164:167], v[72:73], off
	global_load_dwordx4 v[168:171], v[74:75], off
	global_load_dwordx4 v[172:175], v[76:77], off
	global_load_dwordx4 v[176:179], v[126:127], off offset:320
	global_load_dwordx4 v[180:183], v[78:79], off
	global_load_dwordx4 v[184:187], v[80:81], off
	global_load_dwordx4 v[188:191], v[82:83], off
	global_load_dwordx4 v[192:195], v[84:85], off
	global_load_dwordx4 v[196:199], v[86:87], off
	global_load_dwordx4 v[200:203], v[88:89], off
	global_load_dwordx4 v[204:207], v[90:91], off
	global_load_dwordx4 v[208:211], v[92:93], off
	global_load_dwordx4 v[212:215], v[126:127], off offset:384
	global_load_dwordx4 v[216:219], v[94:95], off
	global_load_dwordx4 v[220:223], v[96:97], off
	global_load_dwordx4 v[224:227], v[98:99], off
	global_load_dwordx4 v[228:231], v[100:101], off
	global_load_dwordx4 v[232:235], v[102:103], off
	global_load_dwordx4 v[236:239], v[104:105], off
	global_load_dwordx4 v[240:243], v[106:107], off
	global_load_dwordx4 v[244:247], v[108:109], off
	s_waitcnt vmcnt(25)
	v_mfma_f32_16x16x32_bf16 v[132:135], v[128:131], v[132:135], 0
	s_waitcnt vmcnt(24)
	v_mfma_f32_16x16x32_bf16 v[136:139], v[128:131], v[136:139], 0
	s_waitcnt vmcnt(23)
	v_mfma_f32_16x16x32_bf16 v[140:143], v[128:131], v[140:143], 0
	s_waitcnt vmcnt(22)
	v_mfma_f32_16x16x32_bf16 v[144:147], v[128:131], v[144:147], 0
	s_waitcnt vmcnt(21)
	v_mfma_f32_16x16x32_bf16 v[160:163], v[128:131], v[160:163], 0
	s_waitcnt vmcnt(20)
	v_mfma_f32_16x16x32_bf16 v[164:167], v[128:131], v[164:167], 0
	s_waitcnt vmcnt(19)
	v_mfma_f32_16x16x32_bf16 v[168:171], v[128:131], v[168:171], 0
	s_waitcnt vmcnt(18)
	v_mfma_f32_16x16x32_bf16 v[128:131], v[128:131], v[172:175], 0
	s_waitcnt vmcnt(16)
	v_mfma_f32_16x16x32_bf16 v[132:135], v[176:179], v[180:183], v[132:135]
	s_waitcnt vmcnt(15)
	v_mfma_f32_16x16x32_bf16 v[136:139], v[176:179], v[184:187], v[136:139]
	s_waitcnt vmcnt(14)
	v_mfma_f32_16x16x32_bf16 v[140:143], v[176:179], v[188:191], v[140:143]
	s_waitcnt vmcnt(13)
	v_mfma_f32_16x16x32_bf16 v[144:147], v[176:179], v[192:195], v[144:147]
	s_waitcnt vmcnt(12)
	v_mfma_f32_16x16x32_bf16 v[160:163], v[176:179], v[196:199], v[160:163]
	s_waitcnt vmcnt(11)
	v_mfma_f32_16x16x32_bf16 v[164:167], v[176:179], v[200:203], v[164:167]
	s_waitcnt vmcnt(10)
; #define LAS __attribute__((address_space(3)))
; __device__ __forceinline__ void p11_route(Frame& F) {
;     ...
;             for (int ks = 0; ks < 4; ++ks) { const gbf16x8 a = *(const gbf16x8*)(QRY + (size_t)(t0 + l15) * 2048 + h * 256 + c * 128 + 32 * ks + 8 * g);
; #pragma unroll
;                 for (int nt = 0; nt < 8; ++nt) acc[nt] = __builtin_amdgcn_mfma_f32_16x16x32_bf16(a, *(const gbf16x8*)(SK + ((size_t)(h * 2 + c) * PNK + 16 * nt + l15) * 128 + 32 * ks + 8 * g), acc[nt], 0, 0, 0); }
; #pragma unroll
;             for (int nt = 0; nt < 8; ++nt)
; #pragma unroll
;                 for (int r = 0; r < 4; ++r) sc[(c * 16 + 4 * g + r) * 129 + 16 * nt + l15] = acc[nt][r];
;         }
;         { LAS float* row = sc + (F.lane & 31) * 129; float a[16]; const int nb = (F.lane >> 5) * (PNK / 2);
; #pragma unroll
;             for (int i = 0; i < 16; ++i) a[i] = -INFINITY;
	v_mfma_f32_16x16x32_bf16 v[168:171], v[176:179], v[204:207], v[168:171]
	s_waitcnt vmcnt(9)
	v_mfma_f32_16x16x32_bf16 v[128:131], v[176:179], v[208:211], v[128:131]
	global_load_dwordx4 v[176:179], v[126:127], off offset:448
	global_load_dwordx4 v[180:183], v[110:111], off
	global_load_dwordx4 v[184:187], v[112:113], off
	global_load_dwordx4 v[188:191], v[114:115], off
	global_load_dwordx4 v[192:195], v[116:117], off
	global_load_dwordx4 v[196:199], v[118:119], off
	global_load_dwordx4 v[200:203], v[120:121], off
	global_load_dwordx4 v[204:207], v[122:123], off
	global_load_dwordx4 v[208:211], v[124:125], off
	s_waitcnt vmcnt(16)
	v_mfma_f32_16x16x32_bf16 v[132:135], v[212:215], v[216:219], v[132:135]
	s_waitcnt vmcnt(15)
	v_mfma_f32_16x16x32_bf16 v[136:139], v[212:215], v[220:223], v[136:139]
	s_waitcnt vmcnt(14)
	v_mfma_f32_16x16x32_bf16 v[140:143], v[212:215], v[224:227], v[140:143]
	s_waitcnt vmcnt(13)
	v_mfma_f32_16x16x32_bf16 v[144:147], v[212:215], v[228:231], v[144:147]
	s_waitcnt vmcnt(12)
	v_mfma_f32_16x16x32_bf16 v[160:163], v[212:215], v[232:235], v[160:163]
	s_waitcnt vmcnt(11)
	v_mfma_f32_16x16x32_bf16 v[164:167], v[212:215], v[236:239], v[164:167]
	s_waitcnt vmcnt(10)
	v_mfma_f32_16x16x32_bf16 v[168:171], v[212:215], v[240:243], v[168:171]
	s_waitcnt vmcnt(9)
	v_mfma_f32_16x16x32_bf16 v[128:131], v[212:215], v[244:247], v[128:131]
	s_waitcnt vmcnt(7)
	v_mfma_f32_16x16x32_bf16 v[132:135], v[176:179], v[180:183], v[132:135]
	s_waitcnt vmcnt(6)
	v_mfma_f32_16x16x32_bf16 v[136:139], v[176:179], v[184:187], v[136:139]
	s_waitcnt vmcnt(5)
	v_mfma_f32_16x16x32_bf16 v[140:143], v[176:179], v[188:191], v[140:143]
	s_waitcnt vmcnt(4)
	v_mfma_f32_16x16x32_bf16 v[144:147], v[176:179], v[192:195], v[144:147]
	s_waitcnt vmcnt(3)
	v_mfma_f32_16x16x32_bf16 v[160:163], v[176:179], v[196:199], v[160:163]
	s_waitcnt vmcnt(2)
	v_mfma_f32_16x16x32_bf16 v[164:167], v[176:179], v[200:203], v[164:167]
	s_waitcnt vmcnt(1)
	v_mfma_f32_16x16x32_bf16 v[168:171], v[176:179], v[204:207], v[168:171]
	s_waitcnt vmcnt(0)
	v_mfma_f32_16x16x32_bf16 v[126:129], v[176:179], v[208:211], v[128:131]
	s_nop 2
	v_add_u32_e32 v130, 0x2000, v151
	v_add_u32_e32 v131, 0x2400, v151
	ds_write2_b32 v130, v132, v136 offset0:16 offset1:32
	ds_write2_b32 v130, v133, v137 offset0:145 offset1:161
	ds_write2_b32 v131, v134, v138 offset0:18 offset1:34
	ds_write2_b32 v131, v135, v139 offset0:147 offset1:163
	ds_write2_b32 v130, v140, v144 offset0:48 offset1:64
	ds_write2_b32 v130, v141, v145 offset0:177 offset1:193
	ds_write2_b32 v131, v142, v146 offset0:50 offset1:66
	ds_write2_b32 v131, v143, v147 offset0:179 offset1:195
	ds_write2_b32 v130, v160, v164 offset0:80 offset1:96
	ds_write2_b32 v130, v161, v165 offset0:209 offset1:225
	ds_write2_b32 v131, v162, v166 offset0:82 offset1:98
	ds_write2_b32 v131, v163, v167 offset0:211 offset1:227
	ds_write2_b32 v130, v168, v126 offset0:112 offset1:128
	v_add_u32_e32 v126, 0x2200, v151
	ds_write2_b32 v126, v169, v127 offset0:113 offset1:129
	ds_write2_b32 v131, v170, v128 offset0:114 offset1:130
	v_add_u32_e32 v126, 0x2600, v151
	ds_write2_b32 v126, v171, v129 offset0:115 offset1:131
	v_mov_b32_e32 v137, 0xff800000
	v_mov_b32_e32 v126, v156
	v_mov_b32_e32 v139, 0xff800000
	v_mov_b32_e32 v140, 0xff800000
	v_mov_b32_e32 v141, 0xff800000
	v_mov_b32_e32 v142, 0xff800000
	v_mov_b32_e32 v143, 0xff800000
	v_mov_b32_e32 v144, 0xff800000
	v_mov_b32_e32 v145, 0xff800000
	v_mov_b32_e32 v147, 0xff800000
	v_mov_b32_e32 v161, 0xff800000
	v_mov_b32_e32 v162, 0xff800000
	v_mov_b32_e32 v160, 0xff800000
	v_mov_b32_e32 v129, 0xff800000
